# v34 stack + DIFF attention P.V: transposed V-fragment reads through a 6-buffer ring (5 fragments in flight, counted lgkmcnt) instead of one-ahead on two buffers
# speedup vs baseline: 1.0077x; 1.0032x over previous
.LBB0_842:
	v_exp_f32_e32 v2, v2
	v_exp_f32_e32 v3, v3
	v_exp_f32_e32 v4, v4
	v_exp_f32_e32 v5, v5
	v_exp_f32_e32 v6, v6
	v_exp_f32_e32 v7, v7
	v_exp_f32_e32 v18, v18
	v_exp_f32_e32 v19, v19
	v_exp_f32_e32 v8, v8
	v_exp_f32_e32 v9, v9
	v_exp_f32_e32 v20, v20
	v_exp_f32_e32 v21, v21
	v_pk_add_f32 v[208:209], v[2:3], 0 op_sel_hi:[1,0]
	v_exp_f32_e32 v10, v10
	v_exp_f32_e32 v11, v11
	v_pk_add_f32 v[208:209], v[4:5], v[208:209]
	v_exp_f32_e32 v22, v22
	v_exp_f32_e32 v23, v23
	v_exp_f32_e32 v24, v24
	v_exp_f32_e32 v25, v25
	v_exp_f32_e32 v12, v12
	v_exp_f32_e32 v13, v13
	v_pk_add_f32 v[208:209], v[6:7], v[208:209]
	v_pk_add_f32 v[196:197], v[18:19], 0 op_sel_hi:[1,0]
	v_pk_add_f32 v[208:209], v[8:9], v[208:209]
	v_exp_f32_e32 v26, v26
	v_exp_f32_e32 v27, v27
	v_pk_add_f32 v[196:197], v[20:21], v[196:197]
	v_exp_f32_e32 v28, v28
	v_exp_f32_e32 v29, v29
	v_pk_add_f32 v[208:209], v[10:11], v[208:209]
	v_pk_add_f32 v[196:197], v[22:23], v[196:197]
	v_pk_add_f32 v[212:213], v[12:13], v[208:209]
	v_exp_f32_e32 v30, v30
	v_exp_f32_e32 v31, v31
	v_exp_f32_e32 v14, v14
	v_exp_f32_e32 v15, v15
	v_cvt_pk_f16_f32 v208, v18, v19
	v_cvt_pk_f16_f32 v209, v20, v21
	v_cvt_pk_f16_f32 v210, v22, v23
	v_cvt_pk_f16_f32 v211, v24, v25
	v_pk_add_f32 v[196:197], v[24:25], v[196:197]
	v_exp_f32_e32 v32, v32
	v_exp_f32_e32 v33, v33
	s_waitcnt lgkmcnt(0)
	v_mfma_f32_32x32x16_f16 v[82:97], v[158:161], v[208:211], v[82:97]
	v_exp_f32_e32 v16, v16
	v_exp_f32_e32 v17, v17
	v_pk_add_f32 v[196:197], v[26:27], v[196:197]
	v_pk_add_f32 v[160:161], v[14:15], v[212:213]
	v_pk_add_f32 v[196:197], v[28:29], v[196:197]
	v_pk_add_f32 v[160:161], v[16:17], v[160:161]
	v_pk_add_f32 v[158:159], v[30:31], v[196:197]
	v_mfma_f32_32x32x16_f16 v[66:81], v[154:157], v[208:211], v[66:81]
	v_add_f32_e64 v158, v32, v158
	v_add_f32_e64 v159, v33, v159
	v_cvt_pk_f16_f32 v154, v26, v27
	v_add_f32_e64 v158, v160, v158
	v_add_f32_e64 v159, v161, v159
	v_cvt_pk_f16_f32 v155, v28, v29
	v_add_f32_e32 v195, v158, v159
	v_add_f32_e32 v184, v184, v195
	v_cvt_pk_f16_f32 v156, v30, v31
	v_mfma_f32_32x32x16_f16 v[50:65], v[150:153], v[208:211], v[50:65]
	v_cvt_pk_f16_f32 v157, v32, v33
	v_cvt_pk_f16_f32 v158, v2, v3
	v_cvt_pk_f16_f32 v159, v4, v5
	v_cvt_pk_f16_f32 v160, v6, v7
	v_cvt_pk_f16_f32 v161, v8, v9
	v_cvt_pk_f16_f32 v150, v10, v11
	v_cvt_pk_f16_f32 v151, v12, v13
	v_mfma_f32_32x32x16_f16 v[34:49], v[146:149], v[208:211], v[34:49]
	v_cvt_pk_f16_f32 v152, v14, v15
	v_cvt_pk_f16_f32 v153, v16, v17
	s_and_b64 vcc, exec, s[34:35]
	ds_read_b64_tr_b16 v[146:147], v192 offset:12288
	ds_read_b64_tr_b16 v[148:149], v193 offset:12288
	ds_read_b64_tr_b16 v[196:197], v191 offset:12288
	ds_read_b64_tr_b16 v[198:199], v186 offset:12288
	ds_read_b64_tr_b16 v[212:213], v189 offset:12288
	ds_read_b64_tr_b16 v[214:215], v187 offset:12288
	ds_read_b64_tr_b16 v[216:217], v190 offset:12288
	ds_read_b64_tr_b16 v[218:219], v188 offset:12288
	ds_read_b64_tr_b16 v[220:221], v192 offset:16384
	ds_read_b64_tr_b16 v[222:223], v193 offset:16384
	s_waitcnt lgkmcnt(8)
	v_mfma_f32_32x32x16_f16 v[82:97], v[146:149], v[154:157], v[82:97]
	ds_read_b64_tr_b16 v[224:225], v191 offset:16384
	ds_read_b64_tr_b16 v[226:227], v186 offset:16384
	s_waitcnt lgkmcnt(8)
	v_mfma_f32_32x32x16_f16 v[66:81], v[196:199], v[154:157], v[66:81]
	ds_read_b64_tr_b16 v[146:147], v189 offset:16384
	ds_read_b64_tr_b16 v[148:149], v187 offset:16384
	s_waitcnt lgkmcnt(8)
	v_mfma_f32_32x32x16_f16 v[50:65], v[212:215], v[154:157], v[50:65]
	ds_read_b64_tr_b16 v[196:197], v190 offset:16384
	ds_read_b64_tr_b16 v[198:199], v188 offset:16384
	s_waitcnt lgkmcnt(8)
	v_mfma_f32_32x32x16_f16 v[34:49], v[216:219], v[154:157], v[34:49]
	ds_read_b64_tr_b16 v[212:213], v192 offset:20480
	ds_read_b64_tr_b16 v[214:215], v193 offset:20480
	s_waitcnt lgkmcnt(8)
	v_mfma_f32_32x32x16_f16 v[82:97], v[220:223], v[158:161], v[82:97]
	ds_read_b64_tr_b16 v[216:217], v191 offset:20480
	ds_read_b64_tr_b16 v[218:219], v186 offset:20480
	s_waitcnt lgkmcnt(8)
	v_mfma_f32_32x32x16_f16 v[66:81], v[224:227], v[158:161], v[66:81]
	ds_read_b64_tr_b16 v[220:221], v189 offset:20480
	ds_read_b64_tr_b16 v[222:223], v187 offset:20480
	s_waitcnt lgkmcnt(8)
	v_mfma_f32_32x32x16_f16 v[50:65], v[146:149], v[158:161], v[50:65]
	ds_read_b64_tr_b16 v[224:225], v190 offset:20480
	ds_read_b64_tr_b16 v[226:227], v188 offset:20480
	s_waitcnt lgkmcnt(8)
	v_mfma_f32_32x32x16_f16 v[34:49], v[196:199], v[158:161], v[34:49]
	s_waitcnt lgkmcnt(6)
	v_mfma_f32_32x32x16_f16 v[82:97], v[212:215], v[150:153], v[82:97]
	s_waitcnt lgkmcnt(4)
	v_mfma_f32_32x32x16_f16 v[66:81], v[216:219], v[150:153], v[66:81]
	s_waitcnt lgkmcnt(2)
	v_mfma_f32_32x32x16_f16 v[50:65], v[220:223], v[150:153], v[50:65]
	s_waitcnt lgkmcnt(0)
	v_mfma_f32_32x32x16_f16 v[34:49], v[224:227], v[150:153], v[34:49]
	v_mov_b32_e32 v146, 0
	s_cbranch_vccnz .LBB0_846
	s_mov_b32 s29, 0x41000000
	v_cmp_lg_f32_e64 s[34:35], s1, v194
	v_cmp_lt_f32_e32 vcc, s29, v194
	s_and_b64 s[30:31], s[30:31], s[34:35]
	s_or_b64 s[30:31], vcc, s[30:31]
	v_cndmask_b32_e64 v146, 0, 1, s[30:31]
	v_cmp_ne_u32_e32 vcc, 0, v146
	s_cbranch_vccz .LBB0_845
	v_add_f32_e32 v146, v185, v194
	v_max_f32_e32 v147, v173, v173
	v_max_f32_e32 v173, v147, v146
	v_cmp_neq_f32_e32 vcc, s1, v173
	s_nop 1
	v_cndmask_b32_e32 v146, 0, v173, vcc
	v_sub_f32_e32 v146, v146, v185
	v_exp_f32_e64 v148, -v146
	s_nop 0
	v_pk_mul_f32 v[96:97], v[148:149], v[96:97] op_sel_hi:[0,1]
	v_pk_mul_f32 v[94:95], v[148:149], v[94:95] op_sel_hi:[0,1]
	v_pk_mul_f32 v[92:93], v[148:149], v[92:93] op_sel_hi:[0,1]
	v_pk_mul_f32 v[90:91], v[148:149], v[90:91] op_sel_hi:[0,1]
	v_pk_mul_f32 v[88:89], v[148:149], v[88:89] op_sel_hi:[0,1]
	v_pk_mul_f32 v[86:87], v[148:149], v[86:87] op_sel_hi:[0,1]
	v_pk_mul_f32 v[84:85], v[148:149], v[84:85] op_sel_hi:[0,1]
	v_pk_mul_f32 v[82:83], v[148:149], v[82:83] op_sel_hi:[0,1]
	v_pk_mul_f32 v[80:81], v[148:149], v[80:81] op_sel_hi:[0,1]
	v_pk_mul_f32 v[78:79], v[148:149], v[78:79] op_sel_hi:[0,1]
	v_pk_mul_f32 v[76:77], v[148:149], v[76:77] op_sel_hi:[0,1]
	v_pk_mul_f32 v[74:75], v[148:149], v[74:75] op_sel_hi:[0,1]
	v_pk_mul_f32 v[72:73], v[148:149], v[72:73] op_sel_hi:[0,1]
	v_pk_mul_f32 v[70:71], v[148:149], v[70:71] op_sel_hi:[0,1]
	v_pk_mul_f32 v[68:69], v[148:149], v[68:69] op_sel_hi:[0,1]
	v_pk_mul_f32 v[66:67], v[148:149], v[66:67] op_sel_hi:[0,1]
	v_pk_mul_f32 v[64:65], v[148:149], v[64:65] op_sel_hi:[0,1]
	v_pk_mul_f32 v[62:63], v[148:149], v[62:63] op_sel_hi:[0,1]
	v_pk_mul_f32 v[60:61], v[148:149], v[60:61] op_sel_hi:[0,1]
	v_pk_mul_f32 v[58:59], v[148:149], v[58:59] op_sel_hi:[0,1]
	v_pk_mul_f32 v[56:57], v[148:149], v[56:57] op_sel_hi:[0,1]
	v_pk_mul_f32 v[54:55], v[148:149], v[54:55] op_sel_hi:[0,1]
	v_pk_mul_f32 v[52:53], v[148:149], v[52:53] op_sel_hi:[0,1]
	v_pk_mul_f32 v[50:51], v[148:149], v[50:51] op_sel_hi:[0,1]
	v_pk_mul_f32 v[48:49], v[148:149], v[48:49] op_sel_hi:[0,1]
	v_pk_mul_f32 v[46:47], v[148:149], v[46:47] op_sel_hi:[0,1]
	v_pk_mul_f32 v[44:45], v[148:149], v[44:45] op_sel_hi:[0,1]
	v_pk_mul_f32 v[42:43], v[148:149], v[42:43] op_sel_hi:[0,1]
	v_pk_mul_f32 v[40:41], v[148:149], v[40:41] op_sel_hi:[0,1]
	v_pk_mul_f32 v[38:39], v[148:149], v[38:39] op_sel_hi:[0,1]
	v_pk_mul_f32 v[36:37], v[148:149], v[36:37] op_sel_hi:[0,1]
	v_pk_mul_f32 v[34:35], v[148:149], v[34:35] op_sel_hi:[0,1]
	v_mul_f32_e32 v184, v184, v148
	s_branch .LBB0_846

.LBB0_860:
	v_exp_f32_e32 v98, v98
	v_exp_f32_e32 v99, v99
	v_exp_f32_e32 v100, v100
	v_exp_f32_e32 v101, v101
	v_exp_f32_e32 v102, v102
	v_exp_f32_e32 v103, v103
	v_exp_f32_e32 v114, v114
	v_exp_f32_e32 v115, v115
	v_exp_f32_e32 v104, v104
	v_exp_f32_e32 v105, v105
	v_exp_f32_e32 v116, v116
	v_exp_f32_e32 v117, v117
	v_pk_add_f32 v[208:209], v[98:99], 0 op_sel_hi:[1,0]
	v_exp_f32_e32 v106, v106
	v_exp_f32_e32 v107, v107
	v_pk_add_f32 v[208:209], v[100:101], v[208:209]
	v_exp_f32_e32 v118, v118
	v_exp_f32_e32 v119, v119
	v_exp_f32_e32 v120, v120
	v_exp_f32_e32 v121, v121
	v_exp_f32_e32 v108, v108
	v_exp_f32_e32 v109, v109
	v_pk_add_f32 v[208:209], v[102:103], v[208:209]
	v_pk_add_f32 v[196:197], v[114:115], 0 op_sel_hi:[1,0]
	v_pk_add_f32 v[208:209], v[104:105], v[208:209]
	v_exp_f32_e32 v122, v122
	v_exp_f32_e32 v123, v123
	v_pk_add_f32 v[196:197], v[116:117], v[196:197]
	v_exp_f32_e32 v124, v124
	v_exp_f32_e32 v125, v125
	v_pk_add_f32 v[208:209], v[106:107], v[208:209]
	v_pk_add_f32 v[196:197], v[118:119], v[196:197]
	v_pk_add_f32 v[212:213], v[108:109], v[208:209]
	v_exp_f32_e32 v126, v126
	v_exp_f32_e32 v127, v127
	v_exp_f32_e32 v110, v110
	v_exp_f32_e32 v111, v111
	v_cvt_pk_f16_f32 v208, v114, v115
	v_cvt_pk_f16_f32 v209, v116, v117
	v_cvt_pk_f16_f32 v210, v118, v119
	v_cvt_pk_f16_f32 v211, v120, v121
	v_pk_add_f32 v[196:197], v[120:121], v[196:197]
	v_exp_f32_e32 v128, v128
	v_exp_f32_e32 v129, v129
	s_waitcnt lgkmcnt(0)
	v_mfma_f32_32x32x16_f16 v[82:97], v[158:161], v[208:211], v[82:97]
	v_exp_f32_e32 v112, v112
	v_exp_f32_e32 v113, v113
	v_pk_add_f32 v[196:197], v[122:123], v[196:197]
	v_pk_add_f32 v[160:161], v[110:111], v[212:213]
	v_pk_add_f32 v[196:197], v[124:125], v[196:197]
	v_pk_add_f32 v[160:161], v[112:113], v[160:161]
	v_pk_add_f32 v[158:159], v[126:127], v[196:197]
	v_mfma_f32_32x32x16_f16 v[66:81], v[154:157], v[208:211], v[66:81]
	v_add_f32_e64 v158, v128, v158
	v_add_f32_e64 v159, v129, v159
	v_cvt_pk_f16_f32 v154, v122, v123
	v_add_f32_e64 v158, v158, v160
	v_add_f32_e64 v159, v159, v161
	v_cvt_pk_f16_f32 v155, v124, v125
	v_add_f32_e32 v195, v158, v159
	v_add_f32_e32 v184, v184, v195
	v_cvt_pk_f16_f32 v156, v126, v127
	v_mfma_f32_32x32x16_f16 v[50:65], v[150:153], v[208:211], v[50:65]
	v_cvt_pk_f16_f32 v157, v128, v129
	v_cvt_pk_f16_f32 v158, v98, v99
	v_cvt_pk_f16_f32 v159, v100, v101
	v_cvt_pk_f16_f32 v160, v102, v103
	v_cvt_pk_f16_f32 v161, v104, v105
	v_cvt_pk_f16_f32 v150, v106, v107
	v_cvt_pk_f16_f32 v151, v108, v109
	v_mfma_f32_32x32x16_f16 v[34:49], v[146:149], v[208:211], v[34:49]
	v_cvt_pk_f16_f32 v152, v110, v111
	v_cvt_pk_f16_f32 v153, v112, v113
	s_and_b64 vcc, exec, s[34:35]
	ds_read_b64_tr_b16 v[146:147], v192 offset:12288
	ds_read_b64_tr_b16 v[148:149], v193 offset:12288
	ds_read_b64_tr_b16 v[196:197], v191 offset:12288
	ds_read_b64_tr_b16 v[198:199], v186 offset:12288
	ds_read_b64_tr_b16 v[212:213], v189 offset:12288
	ds_read_b64_tr_b16 v[214:215], v187 offset:12288
	ds_read_b64_tr_b16 v[216:217], v190 offset:12288
	ds_read_b64_tr_b16 v[218:219], v188 offset:12288
	ds_read_b64_tr_b16 v[220:221], v192 offset:16384
	ds_read_b64_tr_b16 v[222:223], v193 offset:16384
	s_waitcnt lgkmcnt(8)
	v_mfma_f32_32x32x16_f16 v[82:97], v[146:149], v[154:157], v[82:97]
	ds_read_b64_tr_b16 v[224:225], v191 offset:16384
	ds_read_b64_tr_b16 v[226:227], v186 offset:16384
	s_waitcnt lgkmcnt(8)
	v_mfma_f32_32x32x16_f16 v[66:81], v[196:199], v[154:157], v[66:81]
	ds_read_b64_tr_b16 v[146:147], v189 offset:16384
	ds_read_b64_tr_b16 v[148:149], v187 offset:16384
	s_waitcnt lgkmcnt(8)
	v_mfma_f32_32x32x16_f16 v[50:65], v[212:215], v[154:157], v[50:65]
	ds_read_b64_tr_b16 v[196:197], v190 offset:16384
	ds_read_b64_tr_b16 v[198:199], v188 offset:16384
	s_waitcnt lgkmcnt(8)
	v_mfma_f32_32x32x16_f16 v[34:49], v[216:219], v[154:157], v[34:49]
	ds_read_b64_tr_b16 v[212:213], v192 offset:20480
	ds_read_b64_tr_b16 v[214:215], v193 offset:20480
	s_waitcnt lgkmcnt(8)
	v_mfma_f32_32x32x16_f16 v[82:97], v[220:223], v[158:161], v[82:97]
	ds_read_b64_tr_b16 v[216:217], v191 offset:20480
	ds_read_b64_tr_b16 v[218:219], v186 offset:20480
	s_waitcnt lgkmcnt(8)
	v_mfma_f32_32x32x16_f16 v[66:81], v[224:227], v[158:161], v[66:81]
	ds_read_b64_tr_b16 v[220:221], v189 offset:20480
	ds_read_b64_tr_b16 v[222:223], v187 offset:20480
	s_waitcnt lgkmcnt(8)
	v_mfma_f32_32x32x16_f16 v[50:65], v[146:149], v[158:161], v[50:65]
	ds_read_b64_tr_b16 v[224:225], v190 offset:20480
	ds_read_b64_tr_b16 v[226:227], v188 offset:20480
	s_waitcnt lgkmcnt(8)
	v_mfma_f32_32x32x16_f16 v[34:49], v[196:199], v[158:161], v[34:49]
	s_waitcnt lgkmcnt(6)
	v_mfma_f32_32x32x16_f16 v[82:97], v[212:215], v[150:153], v[82:97]
	s_waitcnt lgkmcnt(4)
	v_mfma_f32_32x32x16_f16 v[66:81], v[216:219], v[150:153], v[66:81]
	s_waitcnt lgkmcnt(2)
	v_mfma_f32_32x32x16_f16 v[50:65], v[220:223], v[150:153], v[50:65]
	s_waitcnt lgkmcnt(0)
	v_mfma_f32_32x32x16_f16 v[34:49], v[224:227], v[150:153], v[34:49]
	v_mov_b32_e32 v146, 0
	s_cbranch_vccnz .LBB0_865
	s_mov_b32 s29, 0x41000000
	v_cmp_lg_f32_e64 s[34:35], s1, v194
	v_cmp_lt_f32_e32 vcc, s29, v194
	s_and_b64 s[30:31], s[30:31], s[34:35]
	s_or_b64 s[30:31], vcc, s[30:31]
	v_cndmask_b32_e64 v146, 0, 1, s[30:31]
	v_cmp_ne_u32_e32 vcc, 0, v146
	s_cbranch_vccz .LBB0_864
	v_add_f32_e32 v146, v185, v194
	v_max_f32_e32 v147, v173, v173
	v_max_f32_e32 v173, v147, v146
	v_cmp_neq_f32_e32 vcc, s1, v173
	s_nop 1
	v_cndmask_b32_e32 v146, 0, v173, vcc
	v_sub_f32_e32 v146, v146, v185
	v_exp_f32_e64 v148, -v146
	s_nop 0
	v_pk_mul_f32 v[96:97], v[148:149], v[96:97] op_sel_hi:[0,1]
	v_pk_mul_f32 v[94:95], v[148:149], v[94:95] op_sel_hi:[0,1]
	v_pk_mul_f32 v[92:93], v[148:149], v[92:93] op_sel_hi:[0,1]
	v_pk_mul_f32 v[90:91], v[148:149], v[90:91] op_sel_hi:[0,1]
	v_pk_mul_f32 v[88:89], v[148:149], v[88:89] op_sel_hi:[0,1]
	v_pk_mul_f32 v[86:87], v[148:149], v[86:87] op_sel_hi:[0,1]
	v_pk_mul_f32 v[84:85], v[148:149], v[84:85] op_sel_hi:[0,1]
	v_pk_mul_f32 v[82:83], v[148:149], v[82:83] op_sel_hi:[0,1]
	v_pk_mul_f32 v[80:81], v[148:149], v[80:81] op_sel_hi:[0,1]
	v_pk_mul_f32 v[78:79], v[148:149], v[78:79] op_sel_hi:[0,1]
	v_pk_mul_f32 v[76:77], v[148:149], v[76:77] op_sel_hi:[0,1]
	v_pk_mul_f32 v[74:75], v[148:149], v[74:75] op_sel_hi:[0,1]
	v_pk_mul_f32 v[72:73], v[148:149], v[72:73] op_sel_hi:[0,1]
	v_pk_mul_f32 v[70:71], v[148:149], v[70:71] op_sel_hi:[0,1]
	v_pk_mul_f32 v[68:69], v[148:149], v[68:69] op_sel_hi:[0,1]
	v_pk_mul_f32 v[66:67], v[148:149], v[66:67] op_sel_hi:[0,1]
	v_pk_mul_f32 v[64:65], v[148:149], v[64:65] op_sel_hi:[0,1]
	v_pk_mul_f32 v[62:63], v[148:149], v[62:63] op_sel_hi:[0,1]
	v_pk_mul_f32 v[60:61], v[148:149], v[60:61] op_sel_hi:[0,1]
	v_pk_mul_f32 v[58:59], v[148:149], v[58:59] op_sel_hi:[0,1]
	v_pk_mul_f32 v[56:57], v[148:149], v[56:57] op_sel_hi:[0,1]
	v_pk_mul_f32 v[54:55], v[148:149], v[54:55] op_sel_hi:[0,1]
	v_pk_mul_f32 v[52:53], v[148:149], v[52:53] op_sel_hi:[0,1]
	v_pk_mul_f32 v[50:51], v[148:149], v[50:51] op_sel_hi:[0,1]
	v_pk_mul_f32 v[48:49], v[148:149], v[48:49] op_sel_hi:[0,1]
	v_pk_mul_f32 v[46:47], v[148:149], v[46:47] op_sel_hi:[0,1]
	v_pk_mul_f32 v[44:45], v[148:149], v[44:45] op_sel_hi:[0,1]
	v_pk_mul_f32 v[42:43], v[148:149], v[42:43] op_sel_hi:[0,1]
	v_pk_mul_f32 v[40:41], v[148:149], v[40:41] op_sel_hi:[0,1]
	v_pk_mul_f32 v[38:39], v[148:149], v[38:39] op_sel_hi:[0,1]
	v_pk_mul_f32 v[36:37], v[148:149], v[36:37] op_sel_hi:[0,1]
	v_pk_mul_f32 v[34:35], v[148:149], v[34:35] op_sel_hi:[0,1]
	v_mul_f32_e32 v184, v184, v148
	s_branch .LBB0_865

.LBB0_887:
	v_exp_f32_e32 v82, v82
	v_exp_f32_e32 v83, v83
	v_exp_f32_e32 v50, v50
	v_exp_f32_e32 v51, v51
	v_exp_f32_e32 v84, v84
	v_exp_f32_e32 v85, v85
	v_exp_f32_e32 v52, v52
	v_exp_f32_e32 v53, v53
	v_exp_f32_e32 v86, v86
	v_exp_f32_e32 v87, v87
	v_exp_f32_e32 v54, v54
	v_exp_f32_e32 v55, v55
	v_exp_f32_e32 v88, v88
	v_exp_f32_e32 v89, v89
	v_exp_f32_e32 v56, v56
	v_exp_f32_e32 v57, v57
	v_pk_add_f32 v[194:195], v[82:83], 0 op_sel_hi:[1,0]
	v_pk_add_f32 v[196:197], v[50:51], 0 op_sel_hi:[1,0]
	v_exp_f32_e32 v90, v90
	v_exp_f32_e32 v91, v91
	v_exp_f32_e32 v58, v58
	v_exp_f32_e32 v59, v59
	v_pk_add_f32 v[194:195], v[84:85], v[194:195]
	v_pk_add_f32 v[196:197], v[52:53], v[196:197]
	v_exp_f32_e32 v92, v92
	v_exp_f32_e32 v93, v93
	v_exp_f32_e32 v60, v60
	v_exp_f32_e32 v61, v61
	v_pk_add_f32 v[194:195], v[86:87], v[194:195]
	v_pk_add_f32 v[196:197], v[54:55], v[196:197]
	v_pk_add_f32 v[194:195], v[88:89], v[194:195]
	v_pk_add_f32 v[196:197], v[56:57], v[196:197]
	v_pk_add_f32 v[194:195], v[90:91], v[194:195]
	v_pk_add_f32 v[196:197], v[58:59], v[196:197]
	v_pk_add_f32 v[208:209], v[92:93], v[194:195]
	v_pk_add_f32 v[210:211], v[60:61], v[196:197]
	v_exp_f32_e32 v94, v94
	v_exp_f32_e32 v95, v95
	v_exp_f32_e32 v62, v62
	v_exp_f32_e32 v63, v63
	v_cvt_pk_f16_f32 v194, v82, v83
	v_cvt_pk_f16_f32 v195, v84, v85
	v_cvt_pk_f16_f32 v196, v86, v87
	v_cvt_pk_f16_f32 v197, v88, v89
	v_exp_f32_e32 v96, v96
	v_exp_f32_e32 v97, v97
	s_waitcnt lgkmcnt(0)
	v_mfma_f32_32x32x16_f16 v[2:17], v[158:161], v[194:197], v[2:17]
	v_exp_f32_e32 v64, v64
	v_exp_f32_e32 v65, v65
	v_pk_add_f32 v[158:159], v[94:95], v[208:209]
	v_pk_add_f32 v[160:161], v[62:63], v[210:211]
	v_pk_add_f32 v[158:159], v[96:97], v[158:159]
	v_pk_add_f32 v[160:161], v[64:65], v[160:161]
	v_mfma_f32_32x32x16_f16 v[18:33], v[154:157], v[194:197], v[18:33]
	v_add_f32_e64 v158, v160, v158
	v_add_f32_e64 v159, v161, v159
	v_cvt_pk_f16_f32 v154, v90, v91
	v_add_f32_e32 v208, v158, v159
	v_add_f32_e32 v183, v183, v208
	v_cvt_pk_f16_f32 v155, v92, v93
	v_cvt_pk_f16_f32 v156, v94, v95
	v_cvt_pk_f16_f32 v157, v96, v97
	v_mfma_f32_32x32x16_f16 v[34:49], v[150:153], v[194:197], v[34:49]
	v_cvt_pk_f16_f32 v158, v50, v51
	v_cvt_pk_f16_f32 v159, v52, v53
	v_cvt_pk_f16_f32 v160, v54, v55
	v_cvt_pk_f16_f32 v161, v56, v57
	v_cvt_pk_f16_f32 v150, v58, v59
	v_cvt_pk_f16_f32 v151, v60, v61
	v_cvt_pk_f16_f32 v152, v62, v63
	v_mfma_f32_32x32x16_f16 v[66:81], v[146:149], v[194:197], v[66:81]
	v_cvt_pk_f16_f32 v153, v64, v65
	s_and_b64 vcc, exec, s[34:35]
	ds_read_b64_tr_b16 v[146:147], v191 offset:12288
	ds_read_b64_tr_b16 v[148:149], v192 offset:12288
	ds_read_b64_tr_b16 v[208:209], v190 offset:12288
	ds_read_b64_tr_b16 v[210:211], v185 offset:12288
	ds_read_b64_tr_b16 v[212:213], v188 offset:12288
	ds_read_b64_tr_b16 v[214:215], v186 offset:12288
	ds_read_b64_tr_b16 v[216:217], v189 offset:12288
	ds_read_b64_tr_b16 v[218:219], v187 offset:12288
	ds_read_b64_tr_b16 v[220:221], v191 offset:16384
	ds_read_b64_tr_b16 v[222:223], v192 offset:16384
	s_waitcnt lgkmcnt(8)
	v_mfma_f32_32x32x16_f16 v[2:17], v[146:149], v[154:157], v[2:17]
	ds_read_b64_tr_b16 v[224:225], v190 offset:16384
	ds_read_b64_tr_b16 v[226:227], v185 offset:16384
	s_waitcnt lgkmcnt(8)
	v_mfma_f32_32x32x16_f16 v[18:33], v[208:211], v[154:157], v[18:33]
	ds_read_b64_tr_b16 v[146:147], v188 offset:16384
	ds_read_b64_tr_b16 v[148:149], v186 offset:16384
	s_waitcnt lgkmcnt(8)
	v_mfma_f32_32x32x16_f16 v[34:49], v[212:215], v[154:157], v[34:49]
	ds_read_b64_tr_b16 v[208:209], v189 offset:16384
	ds_read_b64_tr_b16 v[210:211], v187 offset:16384
	s_waitcnt lgkmcnt(8)
	v_mfma_f32_32x32x16_f16 v[66:81], v[216:219], v[154:157], v[66:81]
	ds_read_b64_tr_b16 v[212:213], v191 offset:20480
	ds_read_b64_tr_b16 v[214:215], v192 offset:20480
	s_waitcnt lgkmcnt(8)
	v_mfma_f32_32x32x16_f16 v[2:17], v[220:223], v[158:161], v[2:17]
	ds_read_b64_tr_b16 v[216:217], v190 offset:20480
	ds_read_b64_tr_b16 v[218:219], v185 offset:20480
	s_waitcnt lgkmcnt(8)
	v_mfma_f32_32x32x16_f16 v[18:33], v[224:227], v[158:161], v[18:33]
	ds_read_b64_tr_b16 v[220:221], v188 offset:20480
	ds_read_b64_tr_b16 v[222:223], v186 offset:20480
	s_waitcnt lgkmcnt(8)
	v_mfma_f32_32x32x16_f16 v[34:49], v[146:149], v[158:161], v[34:49]
	ds_read_b64_tr_b16 v[224:225], v189 offset:20480
	ds_read_b64_tr_b16 v[226:227], v187 offset:20480
	s_waitcnt lgkmcnt(8)
	v_mfma_f32_32x32x16_f16 v[66:81], v[208:211], v[158:161], v[66:81]
	s_waitcnt lgkmcnt(6)
	v_mfma_f32_32x32x16_f16 v[2:17], v[212:215], v[150:153], v[2:17]
	s_waitcnt lgkmcnt(4)
	v_mfma_f32_32x32x16_f16 v[18:33], v[216:219], v[150:153], v[18:33]
	s_waitcnt lgkmcnt(2)
	v_mfma_f32_32x32x16_f16 v[34:49], v[220:223], v[150:153], v[34:49]
	s_waitcnt lgkmcnt(0)
	v_mfma_f32_32x32x16_f16 v[66:81], v[224:227], v[150:153], v[66:81]
	v_mov_b32_e32 v146, 0
	s_cbranch_vccnz .LBB0_891
	s_mov_b32 s28, 0x41000000
	v_cmp_lg_f32_e64 s[34:35], s1, v193
	v_cmp_lt_f32_e32 vcc, s28, v193
	s_and_b64 s[30:31], s[30:31], s[34:35]
	s_or_b64 s[30:31], vcc, s[30:31]
	v_cndmask_b32_e64 v146, 0, 1, s[30:31]
	v_cmp_ne_u32_e32 vcc, 0, v146
	s_cbranch_vccz .LBB0_890
	v_add_f32_e32 v146, v184, v193
	v_max_f32_e32 v147, v172, v172
	v_max_f32_e32 v172, v147, v146
	v_cmp_neq_f32_e32 vcc, s1, v172
	s_nop 1
	v_cndmask_b32_e32 v146, 0, v172, vcc
	v_sub_f32_e32 v146, v146, v184
	v_exp_f32_e64 v148, -v146
	s_nop 0
	v_pk_mul_f32 v[16:17], v[148:149], v[16:17] op_sel_hi:[0,1]
	v_pk_mul_f32 v[14:15], v[148:149], v[14:15] op_sel_hi:[0,1]
	v_pk_mul_f32 v[12:13], v[148:149], v[12:13] op_sel_hi:[0,1]
	v_pk_mul_f32 v[10:11], v[148:149], v[10:11] op_sel_hi:[0,1]
	v_pk_mul_f32 v[8:9], v[148:149], v[8:9] op_sel_hi:[0,1]
	v_pk_mul_f32 v[6:7], v[148:149], v[6:7] op_sel_hi:[0,1]
	v_pk_mul_f32 v[4:5], v[148:149], v[4:5] op_sel_hi:[0,1]
	v_pk_mul_f32 v[2:3], v[148:149], v[2:3] op_sel_hi:[0,1]
	v_pk_mul_f32 v[32:33], v[148:149], v[32:33] op_sel_hi:[0,1]
	v_pk_mul_f32 v[30:31], v[148:149], v[30:31] op_sel_hi:[0,1]
	v_pk_mul_f32 v[28:29], v[148:149], v[28:29] op_sel_hi:[0,1]
	v_pk_mul_f32 v[26:27], v[148:149], v[26:27] op_sel_hi:[0,1]
	v_pk_mul_f32 v[24:25], v[148:149], v[24:25] op_sel_hi:[0,1]
	v_pk_mul_f32 v[22:23], v[148:149], v[22:23] op_sel_hi:[0,1]
	v_pk_mul_f32 v[20:21], v[148:149], v[20:21] op_sel_hi:[0,1]
	v_pk_mul_f32 v[18:19], v[148:149], v[18:19] op_sel_hi:[0,1]
	v_pk_mul_f32 v[48:49], v[148:149], v[48:49] op_sel_hi:[0,1]
	v_pk_mul_f32 v[46:47], v[148:149], v[46:47] op_sel_hi:[0,1]
	v_pk_mul_f32 v[44:45], v[148:149], v[44:45] op_sel_hi:[0,1]
	v_pk_mul_f32 v[42:43], v[148:149], v[42:43] op_sel_hi:[0,1]
	v_pk_mul_f32 v[40:41], v[148:149], v[40:41] op_sel_hi:[0,1]
	v_pk_mul_f32 v[38:39], v[148:149], v[38:39] op_sel_hi:[0,1]
	v_pk_mul_f32 v[36:37], v[148:149], v[36:37] op_sel_hi:[0,1]
	v_pk_mul_f32 v[34:35], v[148:149], v[34:35] op_sel_hi:[0,1]
	v_pk_mul_f32 v[80:81], v[148:149], v[80:81] op_sel_hi:[0,1]
	v_pk_mul_f32 v[78:79], v[148:149], v[78:79] op_sel_hi:[0,1]
	v_pk_mul_f32 v[76:77], v[148:149], v[76:77] op_sel_hi:[0,1]
	v_pk_mul_f32 v[74:75], v[148:149], v[74:75] op_sel_hi:[0,1]
	v_pk_mul_f32 v[72:73], v[148:149], v[72:73] op_sel_hi:[0,1]
	v_pk_mul_f32 v[70:71], v[148:149], v[70:71] op_sel_hi:[0,1]
	v_pk_mul_f32 v[68:69], v[148:149], v[68:69] op_sel_hi:[0,1]
	v_pk_mul_f32 v[66:67], v[148:149], v[66:67] op_sel_hi:[0,1]
	v_mul_f32_e32 v183, v183, v148
	s_branch .LBB0_891

.LBB0_905:
	v_exp_f32_e32 v114, v114
	v_exp_f32_e32 v115, v115
	v_exp_f32_e32 v98, v98
	v_exp_f32_e32 v99, v99
	v_exp_f32_e32 v116, v116
	v_exp_f32_e32 v117, v117
	v_exp_f32_e32 v100, v100
	v_exp_f32_e32 v101, v101
	v_exp_f32_e32 v118, v118
	v_exp_f32_e32 v119, v119
	v_exp_f32_e32 v102, v102
	v_exp_f32_e32 v103, v103
	v_exp_f32_e32 v120, v120
	v_exp_f32_e32 v121, v121
	v_exp_f32_e32 v104, v104
	v_exp_f32_e32 v105, v105
	v_pk_add_f32 v[194:195], v[114:115], 0 op_sel_hi:[1,0]
	v_pk_add_f32 v[196:197], v[98:99], 0 op_sel_hi:[1,0]
	v_exp_f32_e32 v122, v122
	v_exp_f32_e32 v123, v123
	v_exp_f32_e32 v106, v106
	v_exp_f32_e32 v107, v107
	v_pk_add_f32 v[194:195], v[116:117], v[194:195]
	v_pk_add_f32 v[196:197], v[100:101], v[196:197]
	v_exp_f32_e32 v124, v124
	v_exp_f32_e32 v125, v125
	v_exp_f32_e32 v108, v108
	v_exp_f32_e32 v109, v109
	v_pk_add_f32 v[194:195], v[118:119], v[194:195]
	v_pk_add_f32 v[196:197], v[102:103], v[196:197]
	v_pk_add_f32 v[194:195], v[120:121], v[194:195]
	v_pk_add_f32 v[196:197], v[104:105], v[196:197]
	v_pk_add_f32 v[194:195], v[122:123], v[194:195]
	v_pk_add_f32 v[196:197], v[106:107], v[196:197]
	v_pk_add_f32 v[208:209], v[124:125], v[194:195]
	v_pk_add_f32 v[210:211], v[108:109], v[196:197]
	v_exp_f32_e32 v126, v126
	v_exp_f32_e32 v127, v127
	v_exp_f32_e32 v110, v110
	v_exp_f32_e32 v111, v111
	v_cvt_pk_f16_f32 v194, v114, v115
	v_cvt_pk_f16_f32 v195, v116, v117
	v_cvt_pk_f16_f32 v196, v118, v119
	v_cvt_pk_f16_f32 v197, v120, v121
	v_exp_f32_e32 v128, v128
	v_exp_f32_e32 v129, v129
	s_waitcnt lgkmcnt(0)
	v_mfma_f32_32x32x16_f16 v[2:17], v[158:161], v[194:197], v[2:17]
	v_exp_f32_e32 v112, v112
	v_exp_f32_e32 v113, v113
	v_pk_add_f32 v[158:159], v[126:127], v[208:209]
	v_pk_add_f32 v[160:161], v[110:111], v[210:211]
	v_pk_add_f32 v[158:159], v[128:129], v[158:159]
	v_pk_add_f32 v[160:161], v[112:113], v[160:161]
	v_mfma_f32_32x32x16_f16 v[18:33], v[154:157], v[194:197], v[18:33]
	v_add_f32_e64 v158, v158, v160
	v_add_f32_e64 v159, v159, v161
	v_cvt_pk_f16_f32 v154, v122, v123
	v_add_f32_e32 v208, v158, v159
	v_add_f32_e32 v183, v183, v208
	v_cvt_pk_f16_f32 v155, v124, v125
	v_cvt_pk_f16_f32 v156, v126, v127
	v_cvt_pk_f16_f32 v157, v128, v129
	v_mfma_f32_32x32x16_f16 v[34:49], v[150:153], v[194:197], v[34:49]
	v_cvt_pk_f16_f32 v158, v98, v99
	v_cvt_pk_f16_f32 v159, v100, v101
	v_cvt_pk_f16_f32 v160, v102, v103
	v_cvt_pk_f16_f32 v161, v104, v105
	v_cvt_pk_f16_f32 v150, v106, v107
	v_cvt_pk_f16_f32 v151, v108, v109
	v_cvt_pk_f16_f32 v152, v110, v111
	v_mfma_f32_32x32x16_f16 v[66:81], v[146:149], v[194:197], v[66:81]
	v_cvt_pk_f16_f32 v153, v112, v113
	s_and_b64 vcc, exec, s[34:35]
	ds_read_b64_tr_b16 v[146:147], v191 offset:12288
	ds_read_b64_tr_b16 v[148:149], v192 offset:12288
	ds_read_b64_tr_b16 v[208:209], v190 offset:12288
	ds_read_b64_tr_b16 v[210:211], v185 offset:12288
	ds_read_b64_tr_b16 v[212:213], v188 offset:12288
	ds_read_b64_tr_b16 v[214:215], v186 offset:12288
	ds_read_b64_tr_b16 v[216:217], v189 offset:12288
	ds_read_b64_tr_b16 v[218:219], v187 offset:12288
	ds_read_b64_tr_b16 v[220:221], v191 offset:16384
	ds_read_b64_tr_b16 v[222:223], v192 offset:16384
	s_waitcnt lgkmcnt(8)
	v_mfma_f32_32x32x16_f16 v[2:17], v[146:149], v[154:157], v[2:17]
	ds_read_b64_tr_b16 v[224:225], v190 offset:16384
	ds_read_b64_tr_b16 v[226:227], v185 offset:16384
	s_waitcnt lgkmcnt(8)
	v_mfma_f32_32x32x16_f16 v[18:33], v[208:211], v[154:157], v[18:33]
	ds_read_b64_tr_b16 v[146:147], v188 offset:16384
	ds_read_b64_tr_b16 v[148:149], v186 offset:16384
	s_waitcnt lgkmcnt(8)
	v_mfma_f32_32x32x16_f16 v[34:49], v[212:215], v[154:157], v[34:49]
	ds_read_b64_tr_b16 v[208:209], v189 offset:16384
	ds_read_b64_tr_b16 v[210:211], v187 offset:16384
	s_waitcnt lgkmcnt(8)
	v_mfma_f32_32x32x16_f16 v[66:81], v[216:219], v[154:157], v[66:81]
	ds_read_b64_tr_b16 v[212:213], v191 offset:20480
	ds_read_b64_tr_b16 v[214:215], v192 offset:20480
	s_waitcnt lgkmcnt(8)
	v_mfma_f32_32x32x16_f16 v[2:17], v[220:223], v[158:161], v[2:17]
	ds_read_b64_tr_b16 v[216:217], v190 offset:20480
	ds_read_b64_tr_b16 v[218:219], v185 offset:20480
	s_waitcnt lgkmcnt(8)
	v_mfma_f32_32x32x16_f16 v[18:33], v[224:227], v[158:161], v[18:33]
	ds_read_b64_tr_b16 v[220:221], v188 offset:20480
	ds_read_b64_tr_b16 v[222:223], v186 offset:20480
	s_waitcnt lgkmcnt(8)
	v_mfma_f32_32x32x16_f16 v[34:49], v[146:149], v[158:161], v[34:49]
	ds_read_b64_tr_b16 v[224:225], v189 offset:20480
	ds_read_b64_tr_b16 v[226:227], v187 offset:20480
	s_waitcnt lgkmcnt(8)
	v_mfma_f32_32x32x16_f16 v[66:81], v[208:211], v[158:161], v[66:81]
	s_waitcnt lgkmcnt(6)
	v_mfma_f32_32x32x16_f16 v[2:17], v[212:215], v[150:153], v[2:17]
	s_waitcnt lgkmcnt(4)
	v_mfma_f32_32x32x16_f16 v[18:33], v[216:219], v[150:153], v[18:33]
	s_waitcnt lgkmcnt(2)
	v_mfma_f32_32x32x16_f16 v[34:49], v[220:223], v[150:153], v[34:49]
	s_waitcnt lgkmcnt(0)
	v_mfma_f32_32x32x16_f16 v[66:81], v[224:227], v[150:153], v[66:81]
	v_mov_b32_e32 v146, 0
	s_cbranch_vccnz .LBB0_910
	s_mov_b32 s26, 0x41000000
	v_cmp_lg_f32_e64 s[34:35], s1, v193
	v_cmp_lt_f32_e32 vcc, s26, v193
	s_and_b64 s[30:31], s[30:31], s[34:35]
	s_or_b64 s[30:31], vcc, s[30:31]
	v_cndmask_b32_e64 v146, 0, 1, s[30:31]
	v_cmp_ne_u32_e32 vcc, 0, v146
	s_cbranch_vccz .LBB0_909
	v_add_f32_e32 v146, v184, v193
	v_max_f32_e32 v147, v172, v172
	v_max_f32_e32 v172, v147, v146
	v_cmp_neq_f32_e32 vcc, s1, v172
	s_nop 1
	v_cndmask_b32_e32 v146, 0, v172, vcc
	v_sub_f32_e32 v146, v146, v184
	v_exp_f32_e64 v148, -v146
	s_nop 0
	v_pk_mul_f32 v[16:17], v[148:149], v[16:17] op_sel_hi:[0,1]
	v_pk_mul_f32 v[14:15], v[148:149], v[14:15] op_sel_hi:[0,1]
	v_pk_mul_f32 v[12:13], v[148:149], v[12:13] op_sel_hi:[0,1]
	v_pk_mul_f32 v[10:11], v[148:149], v[10:11] op_sel_hi:[0,1]
	v_pk_mul_f32 v[8:9], v[148:149], v[8:9] op_sel_hi:[0,1]
	v_pk_mul_f32 v[6:7], v[148:149], v[6:7] op_sel_hi:[0,1]
	v_pk_mul_f32 v[4:5], v[148:149], v[4:5] op_sel_hi:[0,1]
	v_pk_mul_f32 v[2:3], v[148:149], v[2:3] op_sel_hi:[0,1]
	v_pk_mul_f32 v[32:33], v[148:149], v[32:33] op_sel_hi:[0,1]
	v_pk_mul_f32 v[30:31], v[148:149], v[30:31] op_sel_hi:[0,1]
	v_pk_mul_f32 v[28:29], v[148:149], v[28:29] op_sel_hi:[0,1]
	v_pk_mul_f32 v[26:27], v[148:149], v[26:27] op_sel_hi:[0,1]
	v_pk_mul_f32 v[24:25], v[148:149], v[24:25] op_sel_hi:[0,1]
	v_pk_mul_f32 v[22:23], v[148:149], v[22:23] op_sel_hi:[0,1]
	v_pk_mul_f32 v[20:21], v[148:149], v[20:21] op_sel_hi:[0,1]
	v_pk_mul_f32 v[18:19], v[148:149], v[18:19] op_sel_hi:[0,1]
	v_pk_mul_f32 v[48:49], v[148:149], v[48:49] op_sel_hi:[0,1]
	v_pk_mul_f32 v[46:47], v[148:149], v[46:47] op_sel_hi:[0,1]
	v_pk_mul_f32 v[44:45], v[148:149], v[44:45] op_sel_hi:[0,1]
	v_pk_mul_f32 v[42:43], v[148:149], v[42:43] op_sel_hi:[0,1]
	v_pk_mul_f32 v[40:41], v[148:149], v[40:41] op_sel_hi:[0,1]
	v_pk_mul_f32 v[38:39], v[148:149], v[38:39] op_sel_hi:[0,1]
	v_pk_mul_f32 v[36:37], v[148:149], v[36:37] op_sel_hi:[0,1]
	v_pk_mul_f32 v[34:35], v[148:149], v[34:35] op_sel_hi:[0,1]
	v_pk_mul_f32 v[80:81], v[148:149], v[80:81] op_sel_hi:[0,1]
	v_pk_mul_f32 v[78:79], v[148:149], v[78:79] op_sel_hi:[0,1]
	v_pk_mul_f32 v[76:77], v[148:149], v[76:77] op_sel_hi:[0,1]
	v_pk_mul_f32 v[74:75], v[148:149], v[74:75] op_sel_hi:[0,1]
	v_pk_mul_f32 v[72:73], v[148:149], v[72:73] op_sel_hi:[0,1]
	v_pk_mul_f32 v[70:71], v[148:149], v[70:71] op_sel_hi:[0,1]
	v_pk_mul_f32 v[68:69], v[148:149], v[68:69] op_sel_hi:[0,1]
	v_pk_mul_f32 v[66:67], v[148:149], v[66:67] op_sel_hi:[0,1]
	v_mul_f32_e32 v183, v183, v148
	s_branch .LBB0_910
